# baseline (speedup 1.0000x reference)
.LBB1_12:
	s_mov_b64 s[36:37], 0x80
	s_add_i32 m0, s57, 0x18000
	v_lshl_add_u64 v[12:13], v[12:13], 0, s[36:37]
	s_waitcnt vmcnt(2)
	s_barrier
	global_load_lds_dwordx4 v[12:13], off
	v_lshl_add_u64 v[10:11], v[10:11], 0, s[36:37]
	s_add_i32 m0, s57, 0x1a000
	s_add_i32 s62, s57, 0x8000
	global_load_lds_dwordx4 v[10:11], off
	v_lshl_add_u64 v[8:9], v[8:9], 0, s[36:37]
	s_mov_b32 m0, s62
	s_add_i32 s63, s57, 0xa000
	global_load_lds_dwordx4 v[8:9], off
	v_lshl_add_u64 v[6:7], v[6:7], 0, s[36:37]
	s_mov_b32 m0, s63
	v_lshl_add_u64 v[4:5], v[4:5], 0, s[36:37]
	global_load_lds_dwordx4 v[6:7], off
	s_add_i32 m0, s57, 0x1c000
	v_lshl_add_u64 v[2:3], v[2:3], 0, s[36:37]
	global_load_lds_dwordx4 v[4:5], off
	s_add_i32 m0, s57, 0x1e000
	s_lshr_b32 s7, s7, 26
	global_load_lds_dwordx4 v[2:3], off
	s_and_b32 s5, s0, 3
	s_add_i32 s7, s6, s7
	s_ashr_i32 s61, s7, 6
	s_lshl_b32 s55, s1, 6
	s_lshl_b32 s1, s1, 13
	s_lshl_b32 s54, s5, 5
	s_cmp_gt_i32 s6, 63
	s_cselect_b64 s[38:39], -1, 0
	s_lshl_b32 s66, s40, 3
	s_lshl_b32 s0, s0, 3
	v_lshlrev_b32_e32 v2, 1, v1
	s_abs_i32 s67, s66
	v_and_or_b32 v144, s0, 8, v2
	v_cvt_f32_u32_e32 v2, s67
	v_lshlrev_b32_e32 v20, 2, v168
	v_lshl_or_b32 v19, v168, 6, v169
	v_and_b32_e32 v20, 32, v20
	v_rcp_iflag_f32_e32 v2, v2
	v_bitop3_b32 v19, v19, s1, v20 bitop3:0xde
	v_lshl_or_b32 v143, s5, 12, v173
	s_ashr_i32 s5, s4, 31
	v_mul_f32_e32 v2, 0x4f7ffffe, v2
	v_cvt_u32_f32_e32 v2, v2
	v_lshlrev_b32_e32 v66, 4, v144
	v_lshl_add_u64 v[154:155], s[22:23], 0, v[66:67]
	s_lshr_b32 s0, s5, 29
	v_readfirstlane_b32 s1, v2
	v_add_u32_e32 v2, v18, v16
	v_mul_lo_u32 v2, s6, v2
	v_lshlrev_b32_e32 v2, 1, v2
	v_add3_u32 v66, v14, v2, v15
	v_add_u32_e32 v2, v17, v16
	s_add_i32 s0, s4, s0
	v_mul_lo_u32 v2, s6, v2
	s_ashr_i32 s68, s0, 3
	s_and_b32 s0, s0, -8
	v_lshlrev_b32_e32 v2, 1, v2
	s_sub_i32 s69, s4, s0
	s_sub_i32 s0, 0, s67
	v_lshl_add_u64 v[156:157], s[30:31], 0, v[66:67]
	v_add3_u32 v66, v14, v2, v15
	s_waitcnt vmcnt(6)
	s_mul_i32 s0, s0, s1
	v_lshl_add_u64 v[158:159], s[30:31], 0, v[66:67]
	v_mov_b32_e32 v66, v67
	v_mov_b32_e32 v68, v67
	v_mov_b32_e32 v69, v67
	s_add_i32 s70, s68, 1
	s_mul_hi_u32 s0, s1, s0
	v_add_u32_e32 v145, 0, v19
	v_mov_b64_e32 v[2:3], v[66:67]
	v_mov_b64_e32 v[6:7], v[66:67]
	v_mov_b64_e32 v[18:19], v[66:67]
	v_mov_b64_e32 v[22:23], v[66:67]
	v_mov_b64_e32 v[34:35], v[66:67]
	v_mov_b64_e32 v[38:39], v[66:67]
	v_mov_b64_e32 v[50:51], v[66:67]
	v_mov_b64_e32 v[54:55], v[66:67]
	v_mov_b64_e32 v[10:11], v[66:67]
	v_mov_b64_e32 v[14:15], v[66:67]
	v_mov_b64_e32 v[26:27], v[66:67]
	v_mov_b64_e32 v[30:31], v[66:67]
	v_mov_b64_e32 v[42:43], v[66:67]
	v_mov_b64_e32 v[46:47], v[66:67]
	v_mov_b64_e32 v[58:59], v[66:67]
	v_mov_b64_e32 v[62:63], v[66:67]
	v_mov_b64_e32 v[72:73], v[68:69]
	v_mov_b64_e32 v[76:77], v[68:69]
	v_mov_b64_e32 v[88:89], v[68:69]
	v_mov_b64_e32 v[92:93], v[68:69]
	v_mov_b64_e32 v[104:105], v[68:69]
	v_mov_b64_e32 v[108:109], v[68:69]
	v_mov_b64_e32 v[120:121], v[68:69]
	v_mov_b64_e32 v[124:125], v[68:69]
	v_mov_b64_e32 v[80:81], v[68:69]
	v_mov_b64_e32 v[84:85], v[68:69]
	v_mov_b64_e32 v[96:97], v[68:69]
	v_mov_b64_e32 v[100:101], v[68:69]
	v_mov_b64_e32 v[112:113], v[68:69]
	v_mov_b64_e32 v[116:117], v[68:69]
	v_mov_b64_e32 v[128:129], v[68:69]
	v_mov_b64_e32 v[132:133], v[68:69]
	s_add_i32 s65, s61, -2
	v_lshlrev_b32_e32 v142, 3, v168
	s_ashr_i32 s64, s2, 31
	s_mul_i32 s71, s70, s69
	s_bfe_i32 s72, s40, 0x1001c
	s_add_i32 s73, s1, s0
	v_mov_b64_e32 v[160:161], s[4:5]
	s_add_i32 s74, 0, 0x10000
	s_add_i32 s75, 0, 0x14000
	v_mov_b64_e32 v[4:5], v[68:69]
	v_mov_b64_e32 v[8:9], v[68:69]
	v_mov_b64_e32 v[20:21], v[68:69]
	v_mov_b64_e32 v[24:25], v[68:69]
	v_mov_b64_e32 v[36:37], v[68:69]
	v_mov_b64_e32 v[40:41], v[68:69]
	v_mov_b64_e32 v[52:53], v[68:69]
	v_mov_b64_e32 v[56:57], v[68:69]
	v_mov_b64_e32 v[12:13], v[68:69]
	v_mov_b64_e32 v[16:17], v[68:69]
	v_mov_b64_e32 v[28:29], v[68:69]
	v_mov_b64_e32 v[32:33], v[68:69]
	v_mov_b64_e32 v[44:45], v[68:69]
	v_mov_b64_e32 v[48:49], v[68:69]
	v_mov_b64_e32 v[60:61], v[68:69]
	v_mov_b64_e32 v[64:65], v[68:69]
	v_mov_b64_e32 v[70:71], v[66:67]
	v_mov_b64_e32 v[74:75], v[66:67]
	v_mov_b64_e32 v[86:87], v[66:67]
	v_mov_b64_e32 v[90:91], v[66:67]
	v_mov_b64_e32 v[102:103], v[66:67]
	v_mov_b64_e32 v[106:107], v[66:67]
	v_mov_b64_e32 v[118:119], v[66:67]
	v_mov_b64_e32 v[122:123], v[66:67]
	v_mov_b64_e32 v[78:79], v[66:67]
	v_mov_b64_e32 v[82:83], v[66:67]
	v_mov_b64_e32 v[94:95], v[66:67]
	v_mov_b64_e32 v[98:99], v[66:67]
	v_mov_b64_e32 v[110:111], v[66:67]
	v_mov_b64_e32 v[114:115], v[66:67]
	v_mov_b64_e32 v[126:127], v[66:67]
	v_mov_b64_e32 v[130:131], v[66:67]
	s_barrier

.LBB1_25:
	v_add_u32_e32 v66, s74, v143
	ds_read_b128 v[134:137], v66
	ds_read_b128 v[138:141], v66 offset:1024
	ds_read_b128 v[162:165], v66 offset:2048
	ds_read_b128 v[178:181], v66 offset:3072
	s_add_i32 s84, s48, 2
	s_add_u32 s50, s4, 0x80
	s_addc_u32 s49, s5, 0
	s_cmp_eq_u32 s65, s48
	s_cselect_b32 s48, s40, s50
	s_cselect_b32 s49, s41, s49
	s_cselect_b32 s51, s43, s83
	s_cselect_b32 s50, s42, s82
	v_lshl_add_u64 v[68:69], s[4:5], 0, v[156:157]
	s_add_i32 m0, s57, 0xc000
	ds_read_b128 v[182:185], v145
	ds_read_b128 v[186:189], v145 offset:1024
	ds_read_b128 v[190:193], v145 offset:2048
	ds_read_b128 v[194:197], v145 offset:3072
	ds_read_b128 v[198:201], v145 offset:4096
	ds_read_b128 v[202:205], v145 offset:5120
	ds_read_b128 v[206:209], v145 offset:6144
	ds_read_b128 v[210:213], v145 offset:7168
	global_load_lds_dwordx4 v[68:69], off
	v_lshl_add_u64 v[68:69], s[4:5], 0, v[158:159]
	s_add_i32 m0, s57, 0xe000
	s_nop 0
	global_load_lds_dwordx4 v[68:69], off
	v_add_u32_e32 v66, s75, v143
	ds_read_b128 v[214:217], v66
	ds_read_b128 v[218:221], v66 offset:1024
	ds_read_b128 v[222:225], v66 offset:2048
	ds_read_b128 v[226:229], v66 offset:3072
	s_waitcnt lgkmcnt(0)
	s_barrier
	s_setprio 1
	v_mfma_f32_16x16x32_f16 v[130:133], v[134:137], v[182:185], v[130:133]
	v_mfma_f32_16x16x32_f16 v[126:129], v[162:165], v[182:185], v[126:129]
	v_mfma_f32_16x16x32_f16 v[114:117], v[134:137], v[190:193], v[114:117]
	v_mfma_f32_16x16x32_f16 v[110:113], v[162:165], v[190:193], v[110:113]
	v_mfma_f32_16x16x32_f16 v[98:101], v[134:137], v[198:201], v[98:101]
	v_mfma_f32_16x16x32_f16 v[94:97], v[162:165], v[198:201], v[94:97]
	v_mfma_f32_16x16x32_f16 v[82:85], v[134:137], v[206:209], v[82:85]
	v_mfma_f32_16x16x32_f16 v[78:81], v[162:165], v[206:209], v[78:81]
	v_mfma_f32_16x16x32_f16 v[130:133], v[138:141], v[186:189], v[130:133]
	v_mfma_f32_16x16x32_f16 v[126:129], v[178:181], v[186:189], v[126:129]
	v_mfma_f32_16x16x32_f16 v[114:117], v[138:141], v[194:197], v[114:117]
	v_mfma_f32_16x16x32_f16 v[110:113], v[178:181], v[194:197], v[110:113]
	v_mfma_f32_16x16x32_f16 v[98:101], v[138:141], v[202:205], v[98:101]
	v_mfma_f32_16x16x32_f16 v[94:97], v[178:181], v[202:205], v[94:97]
	v_mfma_f32_16x16x32_f16 v[82:85], v[138:141], v[210:213], v[82:85]
	v_mfma_f32_16x16x32_f16 v[78:81], v[178:181], v[210:213], v[78:81]
	v_mfma_f32_16x16x32_f16 v[122:125], v[214:217], v[182:185], v[122:125]
	v_mfma_f32_16x16x32_f16 v[118:121], v[222:225], v[182:185], v[118:121]
	v_mfma_f32_16x16x32_f16 v[106:109], v[214:217], v[190:193], v[106:109]
	v_mfma_f32_16x16x32_f16 v[102:105], v[222:225], v[190:193], v[102:105]
	v_mfma_f32_16x16x32_f16 v[90:93], v[214:217], v[198:201], v[90:93]
	v_mfma_f32_16x16x32_f16 v[86:89], v[222:225], v[198:201], v[86:89]
	v_mfma_f32_16x16x32_f16 v[74:77], v[214:217], v[206:209], v[74:77]
	v_mfma_f32_16x16x32_f16 v[68:71], v[222:225], v[206:209], v[70:73]
	v_mfma_f32_16x16x32_f16 v[122:125], v[218:221], v[186:189], v[122:125]
	v_mfma_f32_16x16x32_f16 v[118:121], v[226:229], v[186:189], v[118:121]
	v_mfma_f32_16x16x32_f16 v[106:109], v[218:221], v[194:197], v[106:109]
	v_mfma_f32_16x16x32_f16 v[102:105], v[226:229], v[194:197], v[102:105]
	v_mfma_f32_16x16x32_f16 v[90:93], v[218:221], v[202:205], v[90:93]
	v_mfma_f32_16x16x32_f16 v[86:89], v[226:229], v[202:205], v[86:89]
	v_mfma_f32_16x16x32_f16 v[74:77], v[218:221], v[210:213], v[74:77]
	v_mfma_f32_16x16x32_f16 v[68:71], v[226:229], v[210:213], v[68:71]
	s_setprio 0
	s_barrier
	ds_read_b128 v[182:185], v145 offset:16384
	ds_read_b128 v[186:189], v145 offset:17408
	ds_read_b128 v[190:193], v145 offset:18432
	ds_read_b128 v[194:197], v145 offset:19456
	ds_read_b128 v[198:201], v145 offset:20480
	ds_read_b128 v[202:205], v145 offset:21504
	ds_read_b128 v[206:209], v145 offset:22528
	ds_read_b128 v[210:213], v145 offset:23552
	s_add_i32 s85, s74, s56
	v_lshl_add_u64 v[166:167], s[50:51], 0, v[148:149]
	s_mov_b32 m0, s85
	s_nop 0
	global_load_lds_dwordx4 v[166:167], off
	v_lshl_add_u64 v[230:231], s[50:51], 0, v[152:153]
	s_add_i32 m0, s85, 0x2000
	s_nop 0
	global_load_lds_dwordx4 v[230:231], off
	s_mov_b32 m0, s57
	v_lshl_add_u64 v[232:233], s[48:49], 0, v[146:147]
	global_load_lds_dwordx4 v[232:233], off
	v_lshl_add_u64 v[234:235], s[48:49], 0, v[150:151]
	s_mov_b32 m0, s58
	s_nop 0
	global_load_lds_dwordx4 v[234:235], off
	s_add_u32 s50, s50, s30
	s_addc_u32 s51, s51, s31
	s_add_i32 s85, s75, s56
	v_lshl_add_u64 v[236:237], s[50:51], 0, v[148:149]
	s_mov_b32 m0, s85
	v_lshl_add_u64 v[238:239], s[50:51], 0, v[152:153]
	global_load_lds_dwordx4 v[236:237], off
	s_add_i32 m0, s85, 0x2000
	s_nop 0
	global_load_lds_dwordx4 v[238:239], off
	s_waitcnt vmcnt(6)
	s_waitcnt lgkmcnt(0)
	s_barrier
	s_setprio 1
	v_mfma_f32_16x16x32_f16 v[62:65], v[134:137], v[182:185], v[62:65]
	v_mfma_f32_16x16x32_f16 v[58:61], v[162:165], v[182:185], v[58:61]
	v_mfma_f32_16x16x32_f16 v[46:49], v[134:137], v[190:193], v[46:49]
	v_mfma_f32_16x16x32_f16 v[42:45], v[162:165], v[190:193], v[42:45]
	v_mfma_f32_16x16x32_f16 v[30:33], v[134:137], v[198:201], v[30:33]
	v_mfma_f32_16x16x32_f16 v[26:29], v[162:165], v[198:201], v[26:29]
	v_mfma_f32_16x16x32_f16 v[14:17], v[134:137], v[206:209], v[14:17]
	v_mfma_f32_16x16x32_f16 v[10:13], v[162:165], v[206:209], v[10:13]
	v_mfma_f32_16x16x32_f16 v[62:65], v[138:141], v[186:189], v[62:65]
	v_mfma_f32_16x16x32_f16 v[58:61], v[178:181], v[186:189], v[58:61]
	v_mfma_f32_16x16x32_f16 v[46:49], v[138:141], v[194:197], v[46:49]
	v_mfma_f32_16x16x32_f16 v[42:45], v[178:181], v[194:197], v[42:45]
	v_mfma_f32_16x16x32_f16 v[30:33], v[138:141], v[202:205], v[30:33]
	v_mfma_f32_16x16x32_f16 v[26:29], v[178:181], v[202:205], v[26:29]
	v_mfma_f32_16x16x32_f16 v[14:17], v[138:141], v[210:213], v[14:17]
	v_mfma_f32_16x16x32_f16 v[10:13], v[178:181], v[210:213], v[10:13]
	v_mfma_f32_16x16x32_f16 v[54:57], v[214:217], v[182:185], v[54:57]
	v_mfma_f32_16x16x32_f16 v[50:53], v[222:225], v[182:185], v[50:53]
	v_mfma_f32_16x16x32_f16 v[38:41], v[214:217], v[190:193], v[38:41]
	v_mfma_f32_16x16x32_f16 v[34:37], v[222:225], v[190:193], v[34:37]
	v_mfma_f32_16x16x32_f16 v[22:25], v[214:217], v[198:201], v[22:25]
	v_mfma_f32_16x16x32_f16 v[18:21], v[222:225], v[198:201], v[18:21]
	v_mfma_f32_16x16x32_f16 v[6:9], v[214:217], v[206:209], v[6:9]
	v_mfma_f32_16x16x32_f16 v[2:5], v[222:225], v[206:209], v[2:5]
	v_mfma_f32_16x16x32_f16 v[54:57], v[218:221], v[186:189], v[54:57]
	v_mfma_f32_16x16x32_f16 v[50:53], v[226:229], v[186:189], v[50:53]
	v_mfma_f32_16x16x32_f16 v[38:41], v[218:221], v[194:197], v[38:41]
	v_mfma_f32_16x16x32_f16 v[34:37], v[226:229], v[194:197], v[34:37]
	v_mfma_f32_16x16x32_f16 v[22:25], v[218:221], v[202:205], v[22:25]
	v_mfma_f32_16x16x32_f16 v[18:21], v[226:229], v[202:205], v[18:21]
	v_mfma_f32_16x16x32_f16 v[6:9], v[218:221], v[210:213], v[6:9]
	v_mfma_f32_16x16x32_f16 v[2:5], v[226:229], v[210:213], v[2:5]
	s_setprio 0
	s_barrier
	s_add_i32 s50, 0, 0x18000
	v_add_u32_e32 v66, s50, v143
	ds_read_b128 v[134:137], v66
	ds_read_b128 v[138:141], v66 offset:1024
	ds_read_b128 v[162:165], v66 offset:2048
	ds_read_b128 v[178:181], v66 offset:3072
	s_add_u32 s48, s48, s30
	s_addc_u32 s49, s49, s31
	s_mov_b32 m0, s59
	v_lshl_add_u64 v[72:73], s[48:49], 0, v[146:147]
	ds_read_b128 v[182:185], v145 offset:32768
	ds_read_b128 v[186:189], v145 offset:33792
	ds_read_b128 v[190:193], v145 offset:34816
	ds_read_b128 v[194:197], v145 offset:35840
	ds_read_b128 v[198:201], v145 offset:36864
	ds_read_b128 v[202:205], v145 offset:37888
	ds_read_b128 v[206:209], v145 offset:38912
	ds_read_b128 v[210:213], v145 offset:39936
	global_load_lds_dwordx4 v[72:73], off
	v_lshl_add_u64 v[72:73], s[48:49], 0, v[150:151]
	s_mov_b32 m0, s60
	s_nop 0
	global_load_lds_dwordx4 v[72:73], off
	s_add_i32 s48, 0, 0x1c000
	v_add_u32_e32 v66, s48, v143
	ds_read_b128 v[214:217], v66
	ds_read_b128 v[218:221], v66 offset:1024
	ds_read_b128 v[222:225], v66 offset:2048
	ds_read_b128 v[226:229], v66 offset:3072
	s_waitcnt lgkmcnt(0)
	s_barrier
	s_setprio 1
	v_mfma_f32_16x16x32_f16 v[130:133], v[134:137], v[182:185], v[130:133]
	v_mfma_f32_16x16x32_f16 v[126:129], v[162:165], v[182:185], v[126:129]
	v_mfma_f32_16x16x32_f16 v[114:117], v[134:137], v[190:193], v[114:117]
	v_mfma_f32_16x16x32_f16 v[110:113], v[162:165], v[190:193], v[110:113]
	v_mfma_f32_16x16x32_f16 v[98:101], v[134:137], v[198:201], v[98:101]
	v_mfma_f32_16x16x32_f16 v[94:97], v[162:165], v[198:201], v[94:97]
	v_mfma_f32_16x16x32_f16 v[82:85], v[134:137], v[206:209], v[82:85]
	v_mfma_f32_16x16x32_f16 v[78:81], v[162:165], v[206:209], v[78:81]
	v_mfma_f32_16x16x32_f16 v[130:133], v[138:141], v[186:189], v[130:133]
	v_mfma_f32_16x16x32_f16 v[126:129], v[178:181], v[186:189], v[126:129]
	v_mfma_f32_16x16x32_f16 v[114:117], v[138:141], v[194:197], v[114:117]
	v_mfma_f32_16x16x32_f16 v[110:113], v[178:181], v[194:197], v[110:113]
	v_mfma_f32_16x16x32_f16 v[98:101], v[138:141], v[202:205], v[98:101]
	v_mfma_f32_16x16x32_f16 v[94:97], v[178:181], v[202:205], v[94:97]
	v_mfma_f32_16x16x32_f16 v[82:85], v[138:141], v[210:213], v[82:85]
	v_mfma_f32_16x16x32_f16 v[78:81], v[178:181], v[210:213], v[78:81]
	v_mfma_f32_16x16x32_f16 v[122:125], v[214:217], v[182:185], v[122:125]
	v_mfma_f32_16x16x32_f16 v[118:121], v[222:225], v[182:185], v[118:121]
	v_mfma_f32_16x16x32_f16 v[106:109], v[214:217], v[190:193], v[106:109]
	v_mfma_f32_16x16x32_f16 v[102:105], v[222:225], v[190:193], v[102:105]
	v_mfma_f32_16x16x32_f16 v[90:93], v[214:217], v[198:201], v[90:93]
	v_mfma_f32_16x16x32_f16 v[86:89], v[222:225], v[198:201], v[86:89]
	v_mfma_f32_16x16x32_f16 v[72:75], v[214:217], v[206:209], v[74:77]
	v_mfma_f32_16x16x32_f16 v[68:71], v[222:225], v[206:209], v[68:71]
	v_mfma_f32_16x16x32_f16 v[122:125], v[218:221], v[186:189], v[122:125]
	v_mfma_f32_16x16x32_f16 v[118:121], v[226:229], v[186:189], v[118:121]
	v_mfma_f32_16x16x32_f16 v[106:109], v[218:221], v[194:197], v[106:109]
	v_mfma_f32_16x16x32_f16 v[102:105], v[226:229], v[194:197], v[102:105]
	v_mfma_f32_16x16x32_f16 v[90:93], v[218:221], v[202:205], v[90:93]
	v_mfma_f32_16x16x32_f16 v[86:89], v[226:229], v[202:205], v[86:89]
	v_mfma_f32_16x16x32_f16 v[74:77], v[218:221], v[210:213], v[72:75]
	v_mfma_f32_16x16x32_f16 v[70:73], v[226:229], v[210:213], v[68:71]
	s_setprio 0
	s_barrier
	ds_read_b128 v[182:185], v145 offset:49152
	ds_read_b128 v[186:189], v145 offset:50176
	ds_read_b128 v[190:193], v145 offset:51200
	ds_read_b128 v[194:197], v145 offset:52224
	ds_read_b128 v[198:201], v145 offset:53248
	ds_read_b128 v[202:205], v145 offset:54272
	ds_read_b128 v[206:209], v145 offset:55296
	ds_read_b128 v[210:213], v145 offset:56320
	s_add_i32 s49, s50, s56
	v_lshl_add_u64 v[68:69], v[166:167], 0, s[36:37]
	s_mov_b32 m0, s49
	s_nop 0
	global_load_lds_dwordx4 v[68:69], off
	v_lshl_add_u64 v[68:69], v[230:231], 0, s[36:37]
	s_add_i32 m0, s49, 0x2000
	s_nop 0
	global_load_lds_dwordx4 v[68:69], off
	s_mov_b32 m0, s62
	s_nop 0
	v_lshl_add_u64 v[68:69], v[232:233], 0, s[36:37]
	global_load_lds_dwordx4 v[68:69], off
	v_lshl_add_u64 v[68:69], v[234:235], 0, s[36:37]
	s_mov_b32 m0, s63
	s_nop 0
	global_load_lds_dwordx4 v[68:69], off
	s_add_i32 s48, s48, s56
	v_lshl_add_u64 v[68:69], v[236:237], 0, s[36:37]
	s_mov_b32 m0, s48
	s_nop 0
	global_load_lds_dwordx4 v[68:69], off
	v_lshl_add_u64 v[68:69], v[238:239], 0, s[36:37]
	s_add_i32 m0, s48, 0x2000
	s_nop 0
	global_load_lds_dwordx4 v[68:69], off
	s_waitcnt vmcnt(6)
	s_waitcnt lgkmcnt(0)
	s_barrier
	s_setprio 1
	v_mfma_f32_16x16x32_f16 v[62:65], v[134:137], v[182:185], v[62:65]
	v_mfma_f32_16x16x32_f16 v[58:61], v[162:165], v[182:185], v[58:61]
	v_mfma_f32_16x16x32_f16 v[46:49], v[134:137], v[190:193], v[46:49]
	v_mfma_f32_16x16x32_f16 v[42:45], v[162:165], v[190:193], v[42:45]
	v_mfma_f32_16x16x32_f16 v[30:33], v[134:137], v[198:201], v[30:33]
	v_mfma_f32_16x16x32_f16 v[26:29], v[162:165], v[198:201], v[26:29]
	v_mfma_f32_16x16x32_f16 v[14:17], v[134:137], v[206:209], v[14:17]
	v_mfma_f32_16x16x32_f16 v[10:13], v[162:165], v[206:209], v[10:13]
	v_mfma_f32_16x16x32_f16 v[62:65], v[138:141], v[186:189], v[62:65]
	v_mfma_f32_16x16x32_f16 v[58:61], v[178:181], v[186:189], v[58:61]
	v_mfma_f32_16x16x32_f16 v[46:49], v[138:141], v[194:197], v[46:49]
	v_mfma_f32_16x16x32_f16 v[42:45], v[178:181], v[194:197], v[42:45]
	v_mfma_f32_16x16x32_f16 v[30:33], v[138:141], v[202:205], v[30:33]
	v_mfma_f32_16x16x32_f16 v[26:29], v[178:181], v[202:205], v[26:29]
	v_mfma_f32_16x16x32_f16 v[14:17], v[138:141], v[210:213], v[14:17]
	v_mfma_f32_16x16x32_f16 v[10:13], v[178:181], v[210:213], v[10:13]
	v_mfma_f32_16x16x32_f16 v[54:57], v[214:217], v[182:185], v[54:57]
	v_mfma_f32_16x16x32_f16 v[50:53], v[222:225], v[182:185], v[50:53]
	v_mfma_f32_16x16x32_f16 v[38:41], v[214:217], v[190:193], v[38:41]
	v_mfma_f32_16x16x32_f16 v[34:37], v[222:225], v[190:193], v[34:37]
	v_mfma_f32_16x16x32_f16 v[22:25], v[214:217], v[198:201], v[22:25]
	v_mfma_f32_16x16x32_f16 v[18:21], v[222:225], v[198:201], v[18:21]
	v_mfma_f32_16x16x32_f16 v[6:9], v[214:217], v[206:209], v[6:9]
	v_mfma_f32_16x16x32_f16 v[2:5], v[222:225], v[206:209], v[2:5]
	v_mfma_f32_16x16x32_f16 v[54:57], v[218:221], v[186:189], v[54:57]
	v_mfma_f32_16x16x32_f16 v[50:53], v[226:229], v[186:189], v[50:53]
	v_mfma_f32_16x16x32_f16 v[38:41], v[218:221], v[194:197], v[38:41]
	v_mfma_f32_16x16x32_f16 v[34:37], v[226:229], v[194:197], v[34:37]
	v_mfma_f32_16x16x32_f16 v[22:25], v[218:221], v[202:205], v[22:25]
	v_mfma_f32_16x16x32_f16 v[18:21], v[226:229], v[202:205], v[18:21]
	v_mfma_f32_16x16x32_f16 v[6:9], v[218:221], v[210:213], v[6:9]
	v_mfma_f32_16x16x32_f16 v[2:5], v[226:229], v[210:213], v[2:5]
	s_setprio 0
	s_add_u32 s4, s4, 0x100
	s_addc_u32 s5, s5, 0
	s_add_u32 s82, s82, 0x100
	s_addc_u32 s83, s83, 0
	s_cmp_ge_i32 s84, s61
	s_mov_b32 s48, s84
	s_barrier
	s_cbranch_scc0 .LBB1_25
